# attention loop also stages layer-0 items 0x9800..0xbfff (5 per wave, all 8 waves staging, 4 KiB static LDS for two of the wave tiles); input-projection phase's staging range shortened accordingly
# speedup vs baseline: 1.0194x; 1.0069x over previous
; #define LAS __attribute__((address_space(3)))
;     __device__ __forceinline__ const float* x() const { return (const float*)ld(0); }
;     __device__ __forceinline__ const float* w_gate() const { return (const float*)ld(21); }
;     __device__ __forceinline__ const float* w_up() const { return (const float*)ld(22); }
;     __device__ __forceinline__ const float* w_down() const { return (const float*)ld(23); }
;     __device__ __forceinline__ unsigned char* ws() const { return (unsigned char*)ld(26); }
; __device__ __forceinline__ void convert_moe_items(const Ctx& a, int layer, LAS unsigned char* lds, int it0, int it1, int widx, int nw, int wave, int lane) {
;     LAS float* scr = (LAS float*)(lds + wave * 16384);
;     bf16_t* WGU = (bf16_t*)(a.ws() + WS_WGU + (size_t)layer * WGU_BYTES); bf16_t* WD = (bf16_t*)(a.ws() + WS_WD + (size_t)layer * WD_BYTES);
;     constexpr int I_G = (DM / 64) * (FE / 32), I_D = (FE / 64) * (DM / 32);
;     constexpr int PER_E = 2 * I_G + I_D;
;     const float *wg = a.w_gate(), *wu = a.w_up(), *wd = a.w_down();
;     auto decode = [&](int it) { CvtItem d; const int e = it / PER_E; int r = it % PER_E; const size_t eo = ((size_t)layer * NE + e) * (size_t)DM * FE;
;         if (r < I_G)          { d.src = wg + eo; d.dst = WGU; d.N = FE; d.K = DM; d.row_off = e * 2048; d.ilv = 1; }
;         else if (r < 2 * I_G) { r -= I_G; d.src = wu + eo; d.dst = WGU; d.N = FE; d.K = DM; d.row_off = e * 2048 + 128; d.ilv = 1; }
;         else                  { r -= 2 * I_G; d.src = wd + eo; d.dst = WD; d.N = DM; d.K = FE; d.row_off = e * 2048; d.ilv = 0; }
;         const int nblk = d.N / 32; d.k0 = 64 * (r / nblk); d.n0 = 32 * (r % nblk); return d; };
; PHASE_FN ph_win() { PH_PRO;
;     ...
;     { const int nu = S.total(), maxu = (nu + G - 1) / G, nfull = nu - (maxu - 1) * G;
;       if ((int)blockIdx.x >= nfull && nfull < G) convert_moe_items(a, 0, lds, L0_B, MOE_ITEMS, ((int)blockIdx.x - nfull) * NWAVES + wave, (G - nfull) * NWAVES, wave, lane);
;       else if (nfull >= G) { convert_moe_items(a, 0, lds, L0_B, MOE_ITEMS, gw, NGW, wave, lane); router_prep(a, G, tid, lane, wave); }
;       else router_prep(a, nfull, tid, lane, wave); }
.LBB0_423:
	s_andn2_b64 vcc, exec, s[2:3]
	s_cbranch_vccnz .LBB0_471
	s_sub_i32 s0, s96, s29
	s_lshl_b32 s2, s0, 3
	s_add_i32 s0, 0, 0x23f10
	v_mov_b32_e32 v2, s0
	s_waitcnt vmcnt(0)
	ds_read_b64 v[6:7], v2
	s_add_i32 s0, 0, 0x23ee8
	v_mov_b32_e32 v2, s0
	s_add_i32 s0, 0, 0x23ef8
	ds_read2_b64 v[2:5], v2 offset1:1
	s_waitcnt lgkmcnt(1)
	v_readfirstlane_b32 s4, v6
	v_mov_b32_e32 v6, s0
	v_readfirstlane_b32 s3, v7
	ds_read_b64 v[6:7], v6
	s_add_i32 s2, s2, s58
	s_waitcnt lgkmcnt(1)
	v_readfirstlane_b32 s30, v3
	v_readfirstlane_b32 s31, v2
	v_readfirstlane_b32 s33, v5
	v_readfirstlane_b32 s34, v4
	s_waitcnt lgkmcnt(0)
	v_readfirstlane_b32 s35, v7
	s_cmpk_gt_u32 s2, 0x47ff
	v_readfirstlane_b32 s36, v6
	s_cbranch_scc1 .LBB0_471
	s_add_u32 s0, s4, 0x2530000
	s_addc_u32 s1, s3, 0
	s_add_u32 s4, s4, 0x12530000
	s_addc_u32 s5, s3, 0
	s_add_i32 s39, s2, 0x5000
	s_and_b32 s2, s39, 0xffff
	s_mul_i32 s2, s2, 0xaaab
	s_lshr_b32 s2, s2, 27
	s_mul_i32 s3, s2, 0xc00
	s_sub_i32 s3, s39, s3
	s_and_b32 s10, s3, 0xffff
	s_lshl_b32 s16, s2, 21
	s_lshl_b32 s11, s2, 11
	s_cmpk_gt_u32 s10, 0x3ff
	s_cbranch_scc0 .LBB0_430
	s_cmpk_gt_u32 s10, 0x7ff
	s_cbranch_scc0 .LBB0_436
	s_add_i32 s13, s10, 0xfffff800
	s_lshl_b32 s2, s16, 2
	s_add_u32 s2, s36, s2
	s_addc_u32 s3, s35, 0
	s_mov_b32 s27, 1
	s_cbranch_execz .LBB0_437
	s_movk_i32 s12, 0x800
	s_movk_i32 s37, 0x400
	s_mov_b32 s27, 0
	s_mov_b32 s38, s11
	s_mov_b64 s[6:7], s[4:5]
	s_cbranch_execz .LBB0_431
	s_branch .LBB0_432

; __device__ __forceinline__ void cvt_load(const CvtItem& d, f32x4 (&v)[8], int lane) {
;     const float* p = d.src + (size_t)(d.k0 + (lane >> 3)) * d.N + d.n0 + (lane & 7) * 4;
; #pragma unroll
;     for (int q = 0; q < 8; ++q) v[q] = __builtin_nontemporal_load((const f32x4*)(p + (size_t)(8 * q) * d.N));
; }
; __device__ __forceinline__ void convert_moe_items(const Ctx& a, int layer, LAS unsigned char* lds, int it0, int it1, int widx, int nw, int wave, int lane) {
;     ...
;     int it = it0 + widx;
;     if (it >= it1) return;
;     f32x4 va[8], vb[8]; CvtItem da = decode(it), db = da; bool hb = (it + nw < it1);
;     cvt_load(da, va, lane);
;     if (hb) { db = decode(it + nw); cvt_load(db, vb, lane); }
.LBB0_432:
	s_lshr_b32 s10, s12, 5
	s_ff1_i32_b32 s8, s10
	s_lshr_b32 s8, s13, s8
	s_and_b32 s8, s8, 0xffff
	s_lshl_b32 s8, s8, 6
	v_lshrrev_b32_e32 v70, 3, v214
	s_sub_i32 s9, s47, s29
	s_add_i32 s10, s10, -1
	v_or_b32_e32 v2, s8, v70
	s_lshl_b32 s11, s9, 3
	s_and_b32 s10, s10, s13
	s_mov_b32 s13, 0
	v_mul_hi_u32_u24_e32 v3, s12, v2
	v_mul_u32_u24_e32 v2, s12, v2
	s_lshl_b32 s10, s10, 5
	s_add_i32 s18, s39, s11
	v_lshl_add_u64 v[2:3], v[2:3], 2, s[2:3]
	s_mov_b32 s11, s13
	v_and_b32_e32 v1, 28, v1
	s_cmp_lt_i32 s18, 0x9800
	v_lshl_add_u64 v[2:3], s[10:11], 2, v[2:3]
	v_mov_b32_e32 v67, 0
	v_lshlrev_b32_e32 v66, 2, v1
	s_cselect_b64 s[16:17], -1, 0
	s_lshl_b64 s[20:21], s[12:13], 5
	v_lshl_add_u64 v[10:11], v[2:3], 0, v[66:67]
	v_lshl_add_u64 v[12:13], v[10:11], 0, s[20:21]
	v_lshl_add_u64 v[18:19], v[12:13], 0, s[20:21]
	v_lshl_add_u64 v[20:21], v[18:19], 0, s[20:21]
	v_lshl_add_u64 v[26:27], v[20:21], 0, s[20:21]
	v_lshl_add_u64 v[28:29], v[26:27], 0, s[20:21]
	v_lshl_add_u64 v[34:35], v[28:29], 0, s[20:21]
	global_load_dwordx4 v[2:5], v[10:11], off nt
	global_load_dwordx4 v[6:9], v[12:13], off nt
	s_nop 0
	global_load_dwordx4 v[10:13], v[18:19], off nt
	global_load_dwordx4 v[14:17], v[20:21], off nt
	s_nop 0
	global_load_dwordx4 v[18:21], v[26:27], off nt
	global_load_dwordx4 v[22:25], v[28:29], off nt
	v_lshl_add_u64 v[36:37], v[34:35], 0, s[20:21]
	global_load_dwordx4 v[26:29], v[34:35], off nt
	global_load_dwordx4 v[30:33], v[36:37], off nt
	s_cmp_gt_i32 s18, 0x97ff
	s_mov_b64 s[12:13], s[6:7]
	s_mov_b32 s40, s37
	s_mov_b32 s41, s38
	s_mov_b32 s29, s27
	s_mov_b32 s20, s8
	s_mov_b32 s22, s10
	s_cbranch_scc1 .LBB0_447
	s_mul_hi_i32 s2, s18, 0x2aaaaaab
	s_lshr_b32 s3, s2, 31
	s_ashr_i32 s2, s2, 9
	s_add_i32 s2, s2, s3
	s_mul_i32 s3, s2, 0xc00
	s_sub_i32 s19, s18, s3
	s_ashr_i32 s3, s2, 31
	s_lshl_b64 s[20:21], s[2:3], 21
	s_lshl_b32 s24, s2, 11
	s_cmpk_gt_i32 s19, 0x3ff
	s_cbranch_scc0 .LBB0_438
	s_cmpk_gt_u32 s19, 0x7ff
	s_cbranch_scc0 .LBB0_439
	s_add_i32 s11, s19, 0xfffff800
	s_lshl_b64 s[2:3], s[20:21], 2
	s_add_u32 s2, s36, s2
	s_addc_u32 s3, s35, s3
	s_mov_b64 s[12:13], 0
	s_branch .LBB0_440

; #define LAS __attribute__((address_space(3)))
; __device__ __forceinline__ unsigned pk2(float lo, float hi) { return f2bf(lo) | (f2bf(hi) << 16); }
;     __device__ __forceinline__ const float* x() const { return (const float*)ld(0); }
;     __device__ __forceinline__ const float* c() const { return (const float*)ld(1); }
; template <bool NT = true> __device__ __forceinline__ void cvt_store(const CvtItem& d, const f32x4 (&v)[8], LAS float* scr, int lane) {
;     const int rr = lane >> 3, c4 = (lane & 7) * 4;
; #pragma unroll
;     for (int q = 0; q < 8; ++q) { LAS float* t = scr + (8 * q + rr) * 33 + c4; t[0] = v[q].x; t[1] = v[q].y; t[2] = v[q].z; t[3] = v[q].w; }
;     asm volatile("s_waitcnt lgkmcnt(0)" ::: "memory");
;     const int c = lane & 7;
; #pragma unroll
;     for (int j = 0; j < 4; ++j) { const int n = (lane >> 3) + 8 * j; const LAS float* s = scr + (8 * c) * 33 + n;
;         u32x4 o; o.x = pk2(s[0 * 33], s[1 * 33]); o.y = pk2(s[2 * 33], s[3 * 33]); o.z = pk2(s[4 * 33], s[5 * 33]); o.w = pk2(s[6 * 33], s[7 * 33]);
;         const int ng = d.n0 + n, drow = d.row_off + (d.ilv ? ((ng >> 7) * 256 + (ng & 127)) : ng);
;         if (NT) __builtin_nontemporal_store(o, (u32x4*)(d.dst + (size_t)drow * d.K + d.k0 + 8 * c)); else *(u32x4*)(d.dst + (size_t)drow * d.K + d.k0 + 8 * c) = o; }
;     asm volatile("s_waitcnt lgkmcnt(0)" ::: "memory");
; __device__ __forceinline__ void convert_moe_items(const Ctx& a, int layer, LAS unsigned char* lds, int it0, int it1, int widx, int nw, int wave, int lane) {
;     ...
;         it += 2 * nw; const bool ha = (it < it1);
;         if (ha) { da = decode(it); cvt_load(da, va, lane); }
.Lcvt_p2b_t:
	v_add_u32_e32 v79, 0x420, v74
	v_add_u32_e32 v80, 0x428, v74
	v_add_u32_e32 v81, 0x840, v74
	v_add_u32_e32 v82, 0x848, v74
	v_add_u32_e32 v83, 0xc60, v74
	v_add_u32_e32 v84, 0xc68, v74
	v_add_u32_e32 v85, 0x1080, v74
	v_add_u32_e32 v86, 0x1088, v74
	v_add_u32_e32 v87, 0x14a0, v74
	v_add_u32_e32 v88, 0x14a8, v74
	v_add_u32_e32 v89, 0x18c0, v74
	v_add_u32_e32 v90, 0x18c8, v74
	v_add_u32_e32 v91, 0x1ce0, v74
	v_add_u32_e32 v92, 0x1ce8, v74
	s_waitcnt vmcnt(15)
	ds_write2_b32 v74, v2, v3 offset1:1
	ds_write2_b32 v74, v4, v5 offset0:2 offset1:3
	s_waitcnt vmcnt(14)
	ds_write2_b32 v79, v6, v7 offset1:1
	ds_write2_b32 v80, v8, v9 offset1:1
	s_waitcnt vmcnt(13)
	ds_write2_b32 v81, v10, v11 offset1:1
	ds_write2_b32 v82, v12, v13 offset1:1
	s_waitcnt vmcnt(12)
	ds_write2_b32 v83, v14, v15 offset1:1
	ds_write2_b32 v84, v16, v17 offset1:1
	s_waitcnt vmcnt(11)
	ds_write2_b32 v85, v18, v19 offset1:1
	ds_write2_b32 v86, v20, v21 offset1:1
	s_waitcnt vmcnt(10)
	ds_write2_b32 v87, v22, v23 offset1:1
	ds_write2_b32 v88, v24, v25 offset1:1
	s_waitcnt vmcnt(9)
	ds_write2_b32 v89, v26, v27 offset1:1
	ds_write2_b32 v90, v28, v29 offset1:1
	s_waitcnt vmcnt(8)
	ds_write2_b32 v91, v30, v31 offset1:1
	ds_write2_b32 v92, v32, v33 offset1:1
	s_waitcnt lgkmcnt(0)
	ds_read2_b32 v[98:99], v73 offset1:8
	ds_read2_b32 v[100:101], v73 offset0:33 offset1:41
	ds_read2_b32 v[102:103], v73 offset0:66 offset1:74
	ds_read2_b32 v[104:105], v73 offset0:99 offset1:107
	ds_read2_b32 v[106:107], v73 offset0:132 offset1:140
	s_waitcnt lgkmcnt(4)
	v_bfe_u32 v67, v98, 16, 1
	v_add3_u32 v67, v98, v67, s43
	s_waitcnt lgkmcnt(3)
	v_bfe_u32 v93, v100, 16, 1
	v_lshrrev_b32_e32 v67, 16, v67
	v_add3_u32 v93, v100, v93, s43
	ds_read2_b32 v[108:109], v73 offset0:165 offset1:173
	v_and_or_b32 v94, v93, s44, v67
	s_waitcnt lgkmcnt(3)
	v_bfe_u32 v67, v102, 16, 1
	v_add3_u32 v67, v102, v67, s43
	s_waitcnt lgkmcnt(2)
	v_bfe_u32 v93, v104, 16, 1
	ds_read2_b32 v[110:111], v73 offset0:198 offset1:206
	v_lshrrev_b32_e32 v67, 16, v67
	v_add3_u32 v93, v104, v93, s43
	ds_read2_b32 v[112:113], v73 offset0:231 offset1:239
	v_and_or_b32 v95, v93, s44, v67
	s_waitcnt lgkmcnt(3)
	v_bfe_u32 v67, v106, 16, 1
	v_add3_u32 v67, v106, v67, s43
	s_waitcnt lgkmcnt(2)
	v_bfe_u32 v93, v108, 16, 1
	v_lshrrev_b32_e32 v67, 16, v67
	v_add3_u32 v93, v108, v93, s43
	v_and_or_b32 v96, v93, s44, v67
	s_waitcnt lgkmcnt(1)
	v_bfe_u32 v67, v110, 16, 1
	v_add3_u32 v67, v110, v67, s43
	s_waitcnt lgkmcnt(0)
	v_bfe_u32 v93, v112, 16, 1
	s_cmp_eq_u32 s27, 0
	v_lshrrev_b32_e32 v67, 16, v67
	v_add3_u32 v93, v112, v93, s43
	s_cselect_b64 vcc, -1, 0
	s_lshl_b32 s2, s10, 1
	v_and_or_b32 v97, v93, s44, v67
	s_and_b32 s11, s2, 0xffffff00
	v_bitop3_b32 v93, s10, v75, v70 bitop3:0xc8
	v_or_b32_e32 v67, s10, v70
	v_or_b32_e32 v93, s11, v93
	v_cndmask_b32_e32 v67, v93, v67, vcc
	v_add_u32_e32 v67, s38, v67
	v_mad_u64_u32 v[114:115], s[2:3], v67, s37, 0
	v_ashrrev_i32_e32 v93, 31, v67
	v_mov_b32_e32 v98, v115
	v_mad_u64_u32 v[116:117], s[2:3], v93, s37, v[98:99]
	v_mov_b32_e32 v115, v116
	s_ashr_i32 s9, s8, 31
	v_lshl_add_u64 v[114:115], v[114:115], 1, s[6:7]
	s_lshl_b64 s[2:3], s[8:9], 1
	v_bfe_u32 v67, v99, 16, 1
	v_lshl_add_u64 v[114:115], v[114:115], 0, s[2:3]
	v_add3_u32 v67, v99, v67, s43
	v_bfe_u32 v93, v101, 16, 1
	v_lshl_add_u64 v[114:115], v[114:115], 0, v[68:69]
	v_lshrrev_b32_e32 v67, 16, v67
	v_add3_u32 v93, v101, v93, s43
	global_store_dwordx4 v[114:115], v[94:97], off nt
	s_add_i32 s46, s39, s42
	s_cmp_gt_i32 s46, 0x97ff
	v_and_or_b32 v94, v93, s44, v67
	v_bfe_u32 v67, v103, 16, 1
	v_add3_u32 v67, v103, v67, s43
	v_bfe_u32 v93, v105, 16, 1
	v_lshrrev_b32_e32 v67, 16, v67
	v_add3_u32 v93, v105, v93, s43
	v_and_or_b32 v95, v93, s44, v67
	v_bfe_u32 v67, v107, 16, 1
	v_add3_u32 v67, v107, v67, s43
	v_bfe_u32 v93, v109, 16, 1
	v_lshrrev_b32_e32 v67, 16, v67
	v_add3_u32 v93, v109, v93, s43
	v_and_or_b32 v96, v93, s44, v67
	v_bfe_u32 v67, v111, 16, 1
	v_add3_u32 v67, v111, v67, s43
	v_bfe_u32 v93, v113, 16, 1
	v_lshrrev_b32_e32 v67, 16, v67
	v_add3_u32 v93, v113, v93, s43
	v_and_or_b32 v97, v93, s44, v67
	v_bitop3_b32 v93, s10, v76, v1 bitop3:0xc8
	v_or_b32_e32 v67, s10, v1
	v_or_b32_e32 v93, s11, v93
	v_cndmask_b32_e32 v67, v93, v67, vcc
	v_add_u32_e32 v67, s38, v67
	v_mad_u64_u32 v[98:99], s[24:25], v67, s37, 0
	v_ashrrev_i32_e32 v93, 31, v67
	v_mov_b32_e32 v100, v99
	v_mad_u64_u32 v[100:101], s[24:25], v93, s37, v[100:101]
	v_mov_b32_e32 v99, v100
	v_lshl_add_u64 v[98:99], v[98:99], 1, s[6:7]
	v_lshl_add_u64 v[98:99], v[98:99], 0, s[2:3]
	ds_read2_b32 v[100:101], v73 offset0:16 offset1:24
	v_lshl_add_u64 v[98:99], v[98:99], 0, v[68:69]
	global_store_dwordx4 v[98:99], v[94:97], off nt
	ds_read2_b32 v[98:99], v73 offset0:49 offset1:57
	ds_read2_b32 v[102:103], v73 offset0:82 offset1:90
	ds_read2_b32 v[104:105], v73 offset0:115 offset1:123
	s_waitcnt lgkmcnt(3)
; #define LAS __attribute__((address_space(3)))
; __device__ __forceinline__ unsigned pk2(float lo, float hi) { return f2bf(lo) | (f2bf(hi) << 16); }
;     __device__ __forceinline__ const float* x() const { return (const float*)ld(0); }
;     __device__ __forceinline__ const float* c() const { return (const float*)ld(1); }
; template <bool NT = true> __device__ __forceinline__ void cvt_store(const CvtItem& d, const f32x4 (&v)[8], LAS float* scr, int lane) {
;     ...
;     for (int j = 0; j < 4; ++j) { const int n = (lane >> 3) + 8 * j; const LAS float* s = scr + (8 * c) * 33 + n;
;         u32x4 o; o.x = pk2(s[0 * 33], s[1 * 33]); o.y = pk2(s[2 * 33], s[3 * 33]); o.z = pk2(s[4 * 33], s[5 * 33]); o.w = pk2(s[6 * 33], s[7 * 33]);
;         const int ng = d.n0 + n, drow = d.row_off + (d.ilv ? ((ng >> 7) * 256 + (ng & 127)) : ng);
;         if (NT) __builtin_nontemporal_store(o, (u32x4*)(d.dst + (size_t)drow * d.K + d.k0 + 8 * c)); else *(u32x4*)(d.dst + (size_t)drow * d.K + d.k0 + 8 * c) = o; }
;     asm volatile("s_waitcnt lgkmcnt(0)" ::: "memory");
; __device__ __forceinline__ void convert_moe_items(const Ctx& a, int layer, LAS unsigned char* lds, int it0, int it1, int widx, int nw, int wave, int lane) {
;     ...
;         it += 2 * nw; const bool ha = (it < it1);
;         if (ha) { da = decode(it); cvt_load(da, va, lane); }
;         if (!hb) break;
;         cvt_store(db, vb, scr, lane);
;         hb = (it + nw < it1);
;         if (hb) { db = decode(it + nw); cvt_load(db, vb, lane); }
	v_bfe_u32 v67, v100, 16, 1
	v_add3_u32 v67, v100, v67, s43
	s_waitcnt lgkmcnt(2)
	v_bfe_u32 v93, v98, 16, 1
	ds_read2_b32 v[106:107], v73 offset0:148 offset1:156
	v_lshrrev_b32_e32 v67, 16, v67
	v_add3_u32 v93, v98, v93, s43
	ds_read2_b32 v[108:109], v73 offset0:181 offset1:189
	v_and_or_b32 v94, v93, s44, v67
	s_waitcnt lgkmcnt(3)
	v_bfe_u32 v67, v102, 16, 1
	v_add3_u32 v67, v102, v67, s43
	s_waitcnt lgkmcnt(2)
	v_bfe_u32 v93, v104, 16, 1
	ds_read2_b32 v[110:111], v73 offset0:214 offset1:222
	v_lshrrev_b32_e32 v67, 16, v67
	v_add3_u32 v93, v104, v93, s43
	ds_read2_b32 v[112:113], v73 offset0:247 offset1:255
	v_and_or_b32 v95, v93, s44, v67
	s_waitcnt lgkmcnt(3)
	v_bfe_u32 v67, v106, 16, 1
	v_add3_u32 v67, v106, v67, s43
	s_waitcnt lgkmcnt(2)
	v_bfe_u32 v93, v108, 16, 1
	v_lshrrev_b32_e32 v67, 16, v67
	v_add3_u32 v93, v108, v93, s43
	v_and_or_b32 v96, v93, s44, v67
	s_waitcnt lgkmcnt(1)
	v_bfe_u32 v67, v110, 16, 1
	v_add3_u32 v67, v110, v67, s43
	s_waitcnt lgkmcnt(0)
	v_bfe_u32 v93, v112, 16, 1
	v_lshrrev_b32_e32 v67, 16, v67
	v_add3_u32 v93, v112, v93, s43
	v_and_or_b32 v97, v93, s44, v67
	v_bitop3_b32 v93, s10, v77, v71 bitop3:0xc8
	v_or_b32_e32 v67, s10, v71
	v_or_b32_e32 v93, s11, v93
	v_cndmask_b32_e32 v67, v93, v67, vcc
	v_add_u32_e32 v67, s38, v67
	v_mad_u64_u32 v[114:115], s[24:25], v67, s37, 0
	v_ashrrev_i32_e32 v93, 31, v67
	v_mov_b32_e32 v98, v115
	v_mad_u64_u32 v[116:117], s[24:25], v93, s37, v[98:99]
	v_mov_b32_e32 v115, v116
	v_lshl_add_u64 v[114:115], v[114:115], 1, s[6:7]
	v_bfe_u32 v67, v101, 16, 1
	v_lshl_add_u64 v[114:115], v[114:115], 0, s[2:3]
	v_add3_u32 v67, v101, v67, s43
	v_bfe_u32 v93, v99, 16, 1
	v_lshl_add_u64 v[114:115], v[114:115], 0, v[68:69]
	v_lshrrev_b32_e32 v67, 16, v67
	v_add3_u32 v93, v99, v93, s43
	global_store_dwordx4 v[114:115], v[94:97], off nt
	s_nop 1
	v_and_or_b32 v94, v93, s44, v67
	v_bfe_u32 v67, v103, 16, 1
	v_add3_u32 v67, v103, v67, s43
	v_bfe_u32 v93, v105, 16, 1
	v_lshrrev_b32_e32 v67, 16, v67
	v_add3_u32 v93, v105, v93, s43
	v_and_or_b32 v95, v93, s44, v67
	v_bfe_u32 v67, v107, 16, 1
	v_add3_u32 v67, v107, v67, s43
	v_bfe_u32 v93, v109, 16, 1
	v_lshrrev_b32_e32 v67, 16, v67
	v_add3_u32 v93, v109, v93, s43
	v_and_or_b32 v96, v93, s44, v67
	v_bfe_u32 v67, v111, 16, 1
	v_add3_u32 v67, v111, v67, s43
	v_bfe_u32 v93, v113, 16, 1
	v_lshrrev_b32_e32 v67, 16, v67
	v_add3_u32 v93, v113, v93, s43
	v_and_or_b32 v97, v93, s44, v67
	v_bitop3_b32 v93, s10, v78, v72 bitop3:0xc8
	v_or_b32_e32 v67, s10, v72
	v_or_b32_e32 v93, s11, v93
	v_cndmask_b32_e32 v67, v93, v67, vcc
	v_add_u32_e32 v67, s38, v67
	v_mad_u64_u32 v[98:99], s[24:25], v67, s37, 0
	v_ashrrev_i32_e32 v93, 31, v67
	v_mov_b32_e32 v100, v99
	v_mad_u64_u32 v[100:101], s[24:25], v93, s37, v[100:101]
	v_mov_b32_e32 v99, v100
	v_lshl_add_u64 v[98:99], v[98:99], 1, s[6:7]
	v_lshl_add_u64 v[98:99], v[98:99], 0, s[2:3]
	v_lshl_add_u64 v[98:99], v[98:99], 0, v[68:69]
	global_store_dwordx4 v[98:99], v[94:97], off nt
	s_waitcnt lgkmcnt(0)
	s_cselect_b64 s[24:25], -1, 0
	s_and_b64 vcc, exec, s[24:25]
	s_cbranch_vccnz .LBB0_460
	s_mul_hi_i32 s2, s46, 0x2aaaaaab
	s_lshr_b32 s3, s2, 31
	s_ashr_i32 s2, s2, 9
	s_add_i32 s26, s2, s3
	s_mul_i32 s2, s26, 0xfffff400
	s_ashr_i32 s27, s26, 31
	s_add_i32 s23, s46, s2
	s_lshl_b64 s[8:9], s[26:27], 21
	s_lshl_b32 s47, s26, 11
	s_cmpk_gt_i32 s23, 0x3ff
	s_mov_b64 s[10:11], -1
	s_cbranch_scc0 .LBB0_457
	s_mul_i32 s2, s26, 0xc00
	s_sub_i32 s10, s46, s2
	s_cmpk_gt_u32 s23, 0x7ff
	s_mov_b64 s[6:7], -1
	s_cbranch_scc0 .LBB0_455
	s_add_i32 s21, s10, 0xfffff800
	s_lshl_b64 s[2:3], s[8:9], 2
	s_add_u32 s2, s36, s2
	s_addc_u32 s3, s35, s3
	s_mov_b64 s[6:7], 0

; #define LAS __attribute__((address_space(3)))
; __device__ __forceinline__ unsigned pk2(float lo, float hi) { return f2bf(lo) | (f2bf(hi) << 16); }
;     __device__ __forceinline__ const float* x() const { return (const float*)ld(0); }
;     __device__ __forceinline__ const float* c() const { return (const float*)ld(1); }
; template <bool NT = true> __device__ __forceinline__ void cvt_store(const CvtItem& d, const f32x4 (&v)[8], LAS float* scr, int lane) {
;     const int rr = lane >> 3, c4 = (lane & 7) * 4;
; #pragma unroll
;     for (int q = 0; q < 8; ++q) { LAS float* t = scr + (8 * q + rr) * 33 + c4; t[0] = v[q].x; t[1] = v[q].y; t[2] = v[q].z; t[3] = v[q].w; }
;     asm volatile("s_waitcnt lgkmcnt(0)" ::: "memory");
;     const int c = lane & 7;
; #pragma unroll
;     for (int j = 0; j < 4; ++j) { const int n = (lane >> 3) + 8 * j; const LAS float* s = scr + (8 * c) * 33 + n;
;         u32x4 o; o.x = pk2(s[0 * 33], s[1 * 33]); o.y = pk2(s[2 * 33], s[3 * 33]); o.z = pk2(s[4 * 33], s[5 * 33]); o.w = pk2(s[6 * 33], s[7 * 33]);
;         const int ng = d.n0 + n, drow = d.row_off + (d.ilv ? ((ng >> 7) * 256 + (ng & 127)) : ng);
;         if (NT) __builtin_nontemporal_store(o, (u32x4*)(d.dst + (size_t)drow * d.K + d.k0 + 8 * c)); else *(u32x4*)(d.dst + (size_t)drow * d.K + d.k0 + 8 * c) = o; }
;     asm volatile("s_waitcnt lgkmcnt(0)" ::: "memory");
.Lcvt_p2b_m:
	s_waitcnt vmcnt(12)
	ds_write2_b32 v74, v34, v35 offset1:1
	ds_write2_b32 v74, v36, v37 offset0:2 offset1:3
	ds_write2_b32 v79, v38, v39 offset1:1
	ds_write2_b32 v80, v40, v41 offset1:1
	ds_write2_b32 v81, v42, v43 offset1:1
	ds_write2_b32 v82, v44, v45 offset1:1
	ds_write2_b32 v83, v46, v47 offset1:1
	ds_write2_b32 v84, v48, v49 offset1:1
	ds_write2_b32 v85, v50, v51 offset1:1
	ds_write2_b32 v86, v52, v53 offset1:1
	ds_write2_b32 v87, v54, v55 offset1:1
	ds_write2_b32 v88, v56, v57 offset1:1
	ds_write2_b32 v89, v58, v59 offset1:1
	ds_write2_b32 v90, v60, v61 offset1:1
	ds_write2_b32 v91, v62, v63 offset1:1
	ds_write2_b32 v92, v64, v65 offset1:1
	s_waitcnt lgkmcnt(0)
	ds_read2_b32 v[84:85], v73 offset1:8
	ds_read2_b32 v[86:87], v73 offset0:33 offset1:41
	ds_read2_b32 v[88:89], v73 offset0:66 offset1:74
	ds_read2_b32 v[90:91], v73 offset0:99 offset1:107
	ds_read2_b32 v[92:93], v73 offset0:132 offset1:140
	s_waitcnt lgkmcnt(4)
	v_bfe_u32 v67, v84, 16, 1
	v_add3_u32 v67, v84, v67, s43
	s_waitcnt lgkmcnt(3)
	v_bfe_u32 v79, v86, 16, 1
	v_lshrrev_b32_e32 v67, 16, v67
	v_add3_u32 v79, v86, v79, s43
	ds_read2_b32 v[94:95], v73 offset0:165 offset1:173
	v_and_or_b32 v80, v79, s44, v67
	s_waitcnt lgkmcnt(3)
	v_bfe_u32 v67, v88, 16, 1
	v_add3_u32 v67, v88, v67, s43
	s_waitcnt lgkmcnt(2)
	v_bfe_u32 v79, v90, 16, 1
	ds_read2_b32 v[96:97], v73 offset0:198 offset1:206
	v_lshrrev_b32_e32 v67, 16, v67
	v_add3_u32 v79, v90, v79, s43
	ds_read2_b32 v[98:99], v73 offset0:231 offset1:239
	v_and_or_b32 v81, v79, s44, v67
	s_waitcnt lgkmcnt(3)
	v_bfe_u32 v67, v92, 16, 1
	v_add3_u32 v67, v92, v67, s43
	s_waitcnt lgkmcnt(2)
	v_bfe_u32 v79, v94, 16, 1
	v_lshrrev_b32_e32 v67, 16, v67
	v_add3_u32 v79, v94, v79, s43
	v_and_or_b32 v82, v79, s44, v67
	s_waitcnt lgkmcnt(1)
	v_bfe_u32 v67, v96, 16, 1
	v_add3_u32 v67, v96, v67, s43
	s_waitcnt lgkmcnt(0)
	v_bfe_u32 v79, v98, 16, 1
	v_lshrrev_b32_e32 v67, 16, v67
	v_add3_u32 v79, v98, v79, s43
	v_and_or_b32 v83, v79, s44, v67
	v_add_u32_e32 v67, s22, v70
	s_cmp_eq_u32 s29, 0
	v_lshlrev_b32_e32 v79, 1, v67
	v_and_b32_e32 v84, 0x7f, v67
	v_and_or_b32 v79, v79, s45, v84
	s_cselect_b64 vcc, -1, 0
	v_cndmask_b32_e32 v67, v79, v67, vcc
	v_add_u32_e32 v67, s41, v67
	v_mad_u64_u32 v[100:101], s[2:3], v67, s40, 0
	v_ashrrev_i32_e32 v79, 31, v67
	v_mov_b32_e32 v84, v101
	v_mad_u64_u32 v[102:103], s[2:3], v79, s40, v[84:85]
	v_mov_b32_e32 v101, v102
	s_ashr_i32 s21, s20, 31
	v_lshl_add_u64 v[100:101], v[100:101], 1, s[12:13]
	s_lshl_b64 s[2:3], s[20:21], 1
	v_bfe_u32 v67, v85, 16, 1
	v_lshl_add_u64 v[100:101], v[100:101], 0, s[2:3]
	v_add3_u32 v67, v85, v67, s43
	v_bfe_u32 v79, v87, 16, 1
	v_lshl_add_u64 v[100:101], v[100:101], 0, v[68:69]
	v_lshrrev_b32_e32 v67, 16, v67
	v_add3_u32 v79, v87, v79, s43
	global_store_dwordx4 v[100:101], v[80:83], off nt
	s_nop 1
	v_and_or_b32 v80, v79, s44, v67
	v_bfe_u32 v67, v89, 16, 1
	v_add3_u32 v67, v89, v67, s43
	v_bfe_u32 v79, v91, 16, 1
	v_lshrrev_b32_e32 v67, 16, v67
	v_add3_u32 v79, v91, v79, s43
	v_and_or_b32 v81, v79, s44, v67
	v_bfe_u32 v67, v93, 16, 1
	v_add3_u32 v67, v93, v67, s43
	v_bfe_u32 v79, v95, 16, 1
	v_lshrrev_b32_e32 v67, 16, v67
	v_add3_u32 v79, v95, v79, s43
	v_and_or_b32 v82, v79, s44, v67
	v_bfe_u32 v67, v97, 16, 1
	v_add3_u32 v67, v97, v67, s43
	v_bfe_u32 v79, v99, 16, 1
	v_lshrrev_b32_e32 v67, 16, v67
	v_add3_u32 v79, v99, v79, s43
	v_and_or_b32 v83, v79, s44, v67
	v_add_u32_e32 v67, s22, v1
	v_lshlrev_b32_e32 v79, 1, v67
	v_and_b32_e32 v84, 0x7f, v67
	v_and_or_b32 v79, v79, s45, v84
	v_cndmask_b32_e32 v67, v79, v67, vcc
	v_add_u32_e32 v67, s41, v67
	v_mad_u64_u32 v[84:85], s[16:17], v67, s40, 0
	v_ashrrev_i32_e32 v79, 31, v67
	v_mov_b32_e32 v86, v85
	v_mad_u64_u32 v[86:87], s[16:17], v79, s40, v[86:87]
	v_mov_b32_e32 v85, v86
	v_lshl_add_u64 v[84:85], v[84:85], 1, s[12:13]
	v_lshl_add_u64 v[84:85], v[84:85], 0, s[2:3]
	ds_read2_b32 v[86:87], v73 offset0:16 offset1:24
	v_lshl_add_u64 v[84:85], v[84:85], 0, v[68:69]
	global_store_dwordx4 v[84:85], v[80:83], off nt
	ds_read2_b32 v[84:85], v73 offset0:49 offset1:57
	ds_read2_b32 v[88:89], v73 offset0:82 offset1:90
	ds_read2_b32 v[90:91], v73 offset0:115 offset1:123
	s_waitcnt lgkmcnt(3)
; #define LAS __attribute__((address_space(3)))
; __device__ __forceinline__ unsigned pk2(float lo, float hi) { return f2bf(lo) | (f2bf(hi) << 16); }
;     __device__ __forceinline__ const float* x() const { return (const float*)ld(0); }
;     __device__ __forceinline__ const float* c() const { return (const float*)ld(1); }
; template <bool NT = true> __device__ __forceinline__ void cvt_store(const CvtItem& d, const f32x4 (&v)[8], LAS float* scr, int lane) {
;     ...
;     for (int j = 0; j < 4; ++j) { const int n = (lane >> 3) + 8 * j; const LAS float* s = scr + (8 * c) * 33 + n;
;         u32x4 o; o.x = pk2(s[0 * 33], s[1 * 33]); o.y = pk2(s[2 * 33], s[3 * 33]); o.z = pk2(s[4 * 33], s[5 * 33]); o.w = pk2(s[6 * 33], s[7 * 33]);
;         const int ng = d.n0 + n, drow = d.row_off + (d.ilv ? ((ng >> 7) * 256 + (ng & 127)) : ng);
;         if (NT) __builtin_nontemporal_store(o, (u32x4*)(d.dst + (size_t)drow * d.K + d.k0 + 8 * c)); else *(u32x4*)(d.dst + (size_t)drow * d.K + d.k0 + 8 * c) = o; }
;     asm volatile("s_waitcnt lgkmcnt(0)" ::: "memory");
; __device__ __forceinline__ void convert_moe_items(const Ctx& a, int layer, LAS unsigned char* lds, int it0, int it1, int widx, int nw, int wave, int lane) {
;     ...
;         cvt_store(db, vb, scr, lane);
;         hb = (it + nw < it1);
;         if (hb) { db = decode(it + nw); cvt_load(db, vb, lane); }
;         if (!ha) break;
	v_bfe_u32 v67, v86, 16, 1
	v_add3_u32 v67, v86, v67, s43
	s_waitcnt lgkmcnt(2)
	v_bfe_u32 v79, v84, 16, 1
	ds_read2_b32 v[92:93], v73 offset0:148 offset1:156
	v_lshrrev_b32_e32 v67, 16, v67
	v_add3_u32 v79, v84, v79, s43
	ds_read2_b32 v[94:95], v73 offset0:181 offset1:189
	v_and_or_b32 v80, v79, s44, v67
	s_waitcnt lgkmcnt(3)
	v_bfe_u32 v67, v88, 16, 1
	v_add3_u32 v67, v88, v67, s43
	s_waitcnt lgkmcnt(2)
	v_bfe_u32 v79, v90, 16, 1
	ds_read2_b32 v[96:97], v73 offset0:214 offset1:222
	v_lshrrev_b32_e32 v67, 16, v67
	v_add3_u32 v79, v90, v79, s43
	ds_read2_b32 v[98:99], v73 offset0:247 offset1:255
	v_and_or_b32 v81, v79, s44, v67
	s_waitcnt lgkmcnt(3)
	v_bfe_u32 v67, v92, 16, 1
	v_add3_u32 v67, v92, v67, s43
	s_waitcnt lgkmcnt(2)
	v_bfe_u32 v79, v94, 16, 1
	v_lshrrev_b32_e32 v67, 16, v67
	v_add3_u32 v79, v94, v79, s43
	v_and_or_b32 v82, v79, s44, v67
	s_waitcnt lgkmcnt(1)
	v_bfe_u32 v67, v96, 16, 1
	v_add3_u32 v67, v96, v67, s43
	s_waitcnt lgkmcnt(0)
	v_bfe_u32 v79, v98, 16, 1
	v_lshrrev_b32_e32 v67, 16, v67
	v_add3_u32 v79, v98, v79, s43
	v_and_or_b32 v83, v79, s44, v67
	v_add_u32_e32 v67, s22, v71
	v_lshlrev_b32_e32 v79, 1, v67
	v_and_b32_e32 v84, 0x7f, v67
	v_and_or_b32 v79, v79, s45, v84
	v_cndmask_b32_e32 v67, v79, v67, vcc
	v_add_u32_e32 v67, s41, v67
	v_mad_u64_u32 v[100:101], s[16:17], v67, s40, 0
	v_ashrrev_i32_e32 v79, 31, v67
	v_mov_b32_e32 v84, v101
	v_mad_u64_u32 v[102:103], s[16:17], v79, s40, v[84:85]
	v_mov_b32_e32 v101, v102
	v_lshl_add_u64 v[100:101], v[100:101], 1, s[12:13]
	v_bfe_u32 v67, v87, 16, 1
	v_lshl_add_u64 v[100:101], v[100:101], 0, s[2:3]
	v_add3_u32 v67, v87, v67, s43
	v_bfe_u32 v79, v85, 16, 1
	v_lshl_add_u64 v[100:101], v[100:101], 0, v[68:69]
	v_lshrrev_b32_e32 v67, 16, v67
	v_add3_u32 v79, v85, v79, s43
	global_store_dwordx4 v[100:101], v[80:83], off nt
	s_nop 1
	v_and_or_b32 v80, v79, s44, v67
	v_bfe_u32 v67, v89, 16, 1
	v_add3_u32 v67, v89, v67, s43
	v_bfe_u32 v79, v91, 16, 1
	v_lshrrev_b32_e32 v67, 16, v67
	v_add3_u32 v79, v91, v79, s43
	v_and_or_b32 v81, v79, s44, v67
	v_bfe_u32 v67, v93, 16, 1
	v_add3_u32 v67, v93, v67, s43
	v_bfe_u32 v79, v95, 16, 1
	v_lshrrev_b32_e32 v67, 16, v67
	v_add3_u32 v79, v95, v79, s43
	v_and_or_b32 v82, v79, s44, v67
	v_bfe_u32 v67, v97, 16, 1
	v_add3_u32 v67, v97, v67, s43
	v_bfe_u32 v79, v99, 16, 1
	v_lshrrev_b32_e32 v67, 16, v67
	v_add3_u32 v79, v99, v79, s43
	v_and_or_b32 v83, v79, s44, v67
	v_add_u32_e32 v67, s22, v72
	v_lshlrev_b32_e32 v79, 1, v67
	v_and_b32_e32 v84, 0x7f, v67
	v_and_or_b32 v79, v79, s45, v84
	v_cndmask_b32_e32 v67, v79, v67, vcc
	v_add_u32_e32 v67, s41, v67
	v_mad_u64_u32 v[84:85], s[16:17], v67, s40, 0
	v_ashrrev_i32_e32 v79, 31, v67
	v_mov_b32_e32 v86, v85
	v_mad_u64_u32 v[86:87], s[16:17], v79, s40, v[86:87]
	v_mov_b32_e32 v85, v86
	v_lshl_add_u64 v[84:85], v[84:85], 1, s[12:13]
	v_lshl_add_u64 v[84:85], v[84:85], 0, s[2:3]
	v_lshl_add_u64 v[84:85], v[84:85], 0, v[68:69]
	global_store_dwordx4 v[84:85], v[80:83], off nt
	s_add_i32 s2, s28, s39
	s_addk_i32 s2, 0xebc0
	s_waitcnt lgkmcnt(0)
	s_cmp_lt_i32 s2, 0x9800
	s_cselect_b64 s[16:17], -1, 0
	s_cmp_gt_i32 s2, 0x97ff
	s_cbranch_scc1 .LBB0_449
	s_mul_hi_i32 s3, s2, 0x2aaaaaab
	s_lshr_b32 s9, s3, 31
	s_ashr_i32 s3, s3, 9
	s_add_i32 s12, s3, s9
	s_mul_i32 s3, s12, 0xc00
	s_ashr_i32 s13, s12, 31
	s_sub_i32 s11, s2, s3
	s_lshl_b64 s[20:21], s[12:13], 21
	s_lshl_b32 s26, s12, 11
	s_cmpk_gt_i32 s11, 0x3ff
	s_mov_b64 s[22:23], -1
	s_cbranch_scc0 .LBB0_467
	s_cmpk_gt_u32 s11, 0x7ff
	s_mov_b64 s[12:13], -1
	s_cbranch_scc0 .LBB0_465
	s_add_i32 s9, s11, 0xfffff800
	s_lshl_b64 s[2:3], s[20:21], 2
	s_add_u32 s2, s36, s2
	s_addc_u32 s3, s35, s3
	s_mov_b64 s[12:13], 0

; #define LAS __attribute__((address_space(3)))
; #define WAIT_BAR(N) asm volatile("s_waitcnt vmcnt(" #N ") lgkmcnt(0)\n\ts_barrier" ::: "memory")
; #define DMA_K(t, slot) do { const bf16_t* sb_ = Kh + (long)(t) * KVBLK * DMK; glds16<0>(sb_, kvoff, (unsigned)__builtin_amdgcn_readfirstlane(kdst + (slot))); glds16<0>(sb_ + 64, kvoff, (unsigned)__builtin_amdgcn_readfirstlane(kdst + 8192 + (slot))); } while (0)
; template <int THRL> ...
;     ...
;   const bf16_t* Qw = Q + (size_t)(CTXL + qb * 128 + wq * QBLK) * DMK + head * 128 + comp * 64;
;   const bf16_t* Kh = K + head * 128; const bf16_t* Vh = V + head * 128;
;   const unsigned lds0 = (unsigned)(uintptr_t)shm;
;   LAS float* wsf = (LAS float*)(shm + LDS_WS) + wid * 64;
;   const unsigned kvoff = (unsigned)(lane * DMK + wid * 8) * 2u;
;   const unsigned vvoff = (unsigned)((16 * (wid & 3) + (lane >> 2)) * DMK + (wid >> 2) * 32 + (lane & 3) * 8) * 2u;
;   const unsigned kdst = lds0 + LDS_K + wid * 1024, vdst = lds0 + LDS_V + wid * 1024;
;     ...
;   const int vb0 = (int)(lds0 + LDS_V) + ((lane >> 4) & 1) * 32 + (lane & 3) * 8 + (4 * hi + ((lane & 15) >> 2)) * 64;
;   bf16x8 kf[8];
;   const lds_cptr shm3 = (lds_cptr)shm; const lds_cptr kp0 = shm3 + LDS_K + comp * 8192 + hi * 1024 + r32 * 16;
;   const lds_cptr vp0 = shm3 + LDS_V + ((lane >> 4) & 1) * 32 + (lane & 3) * 8 + (4 * hi + ((lane & 15) >> 2)) * 64;
;   DMA_K(0, 0); DMA_V(0, 0); DMA_K(1, SLOTB);
;   bf16x8 qr[4];
; #pragma unroll
;   for (int d0 = 0; d0 < 4; ++d0) qr[d0] = *reinterpret_cast<const bf16x8*>(&Qw[(long)r32 * DMK + d0 * 16 + hi * 8]);
;   float mhat = 0.f, l_reg = 0.f; f32x16 o[4]; o[0] = f32x16{}; o[1] = f32x16{}; o[2] = f32x16{}; o[3] = f32x16{}; f32x16 negm = f32x16{}; asm volatile("" : "+v"(negm));
;   bool resc = false;
;     ...
;   f32x16 pA0, pA1, pB0, pB1;
;   int sl_prev = 0, sl_cur = 0, sl_next = SLOTB;
;     ...
;   DMA_K(2, 2 * SLOTB);
;   WAIT_BAR(6);
;   qkt(pA0, pA1, kp0, qr, negm); asm volatile("s_nop 15\n\ts_nop 7" : "+v"(pA0), "+v"(pA1));
;   const lds_cptr qp = shm3 + LDS_Q + wid * 4096 + lane * 16;
; #pragma unroll
;   for (int d0 = 0; d0 < 4; ++d0) *(LAS bf16x8*)(shm + LDS_Q + wid * 4096 + lane * 16 + d0 * 1024) = qr[d0];
;   START(pA0, pA1);
.LBB0_527:
	s_lshl_b32 s0, s28, 1
	s_and_b32 s0, s0, 0x700
	s_add_u32 s33, s26, s0
	s_addc_u32 s53, s27, 0
	s_bfe_u32 s41, s39, 0x20006
	s_lshl_b32 s0, s36, 4
	s_and_b32 s37, s0, 0xffffff80
	s_lshl_b32 s0, s41, 5
	s_or_b32 s0, s37, s0
	s_addk_i32 s0, 0x100
	s_ashr_i32 s1, s0, 31
	s_lshr_b32 s40, s39, 6
	s_lshr_b32 s42, s39, 8
	s_lshl_b64 s[0:1], s[0:1], 11
	s_add_u32 s0, s5, s0
	s_addc_u32 s1, s17, s1
	s_lshl_b32 s2, s36, 7
	s_and_b32 s14, s2, 0x380
	s_lshl_b32 s8, s14, 1
	s_add_u32 s0, s0, s8
	s_addc_u32 s1, s1, 0
	s_lshl_b32 s43, s42, 6
	s_lshl_b32 s2, s42, 7
	s_add_u32 s2, s0, s2
	s_addc_u32 s3, s1, 0
	s_add_u32 s20, s22, s8
	s_addc_u32 s21, s23, 0
	s_add_u32 s8, s24, s8
	s_addc_u32 s9, s25, 0
	s_lshl_b32 s0, s41, 15
	s_add_i32 s0, s0, s43
	v_add_u32_e32 v235, s0, v219
	s_lshl_b32 s0, s40, 10
	s_add_i32 s49, s0, 0
	s_and_b32 s1, s39, 0x3fffffc0
	s_lshl_b32 s38, s40, 4
	s_add_i32 s46, s49, 0xc000
	s_add_u32 s44, s20, 0x80
	v_add_u32_e32 v237, s38, v218
	s_mov_b32 s0, m0
	s_mov_b32 m0, s49
	s_nop 0
	global_load_lds_dwordx4 v237, s[20:21] offset:0
	s_mov_b32 m0, s0
	s_addc_u32 s45, s21, 0
	s_add_i32 s54, s49, 0x2000
	s_mov_b32 s0, m0
	s_mov_b32 m0, s54
	s_nop 0
	global_load_lds_dwordx4 v237, s[44:45] offset:0
	s_mov_b32 m0, s0
	s_add_u32 s50, s8, 0x80
	s_mov_b32 s0, m0
	s_mov_b32 m0, s46
	s_nop 0
	global_load_lds_dwordx4 v235, s[8:9] offset:0
	s_mov_b32 m0, s0
	s_addc_u32 s51, s9, 0
	s_add_i32 s45, s49, 0xe000
	s_mov_b32 s0, m0
	s_mov_b32 m0, s45
	s_nop 0
	global_load_lds_dwordx4 v235, s[50:51] offset:0
	s_mov_b32 m0, s0
	s_add_u32 s50, s20, 0x20000
	s_addc_u32 s51, s21, 0
	s_add_i32 s52, s49, 0x4000
	s_mov_b32 s0, m0
	s_mov_b32 m0, s52
	s_nop 0
	global_load_lds_dwordx4 v237, s[50:51] offset:0
	s_mov_b32 m0, s0
	s_add_u32 s56, s20, 0x20080
	s_addc_u32 s57, s21, 0
	s_add_i32 s51, s49, 0x6000
	s_mov_b32 s0, m0
	s_mov_b32 m0, s51
	s_nop 0
	global_load_lds_dwordx4 v237, s[56:57] offset:0
	s_mov_b32 m0, s0
	global_load_dwordx4 v[66:69], v229, s[2:3]
	global_load_dwordx4 v[70:73], v229, s[2:3] offset:32
	global_load_dwordx4 v[74:77], v229, s[2:3] offset:64
	global_load_dwordx4 v[78:81], v229, s[2:3] offset:96
	v_mov_b64_e32 v[48:49], v[32:33]
	s_add_u32 s2, s20, 0x40000
	v_mov_b64_e32 v[46:47], v[30:31]
	v_mov_b64_e32 v[44:45], v[28:29]
	v_mov_b64_e32 v[42:43], v[26:27]
	v_mov_b64_e32 v[40:41], v[24:25]
	v_mov_b64_e32 v[38:39], v[22:23]
	v_mov_b64_e32 v[36:37], v[20:21]
	v_mov_b64_e32 v[34:35], v[18:19]
	s_addc_u32 s3, s21, 0
	s_add_i32 s48, s49, 0x8000
	s_mov_b32 s0, m0
	s_mov_b32 m0, s48
	s_nop 0
	global_load_lds_dwordx4 v237, s[2:3] offset:0
	s_mov_b32 m0, s0
	s_add_u32 s2, s20, 0x40080
	s_addc_u32 s3, s21, 0
	s_add_i32 s47, s49, 0xa000
	s_mov_b32 s0, m0
	s_mov_b32 m0, s47
	s_nop 0
	global_load_lds_dwordx4 v237, s[2:3] offset:0
	s_mov_b32 m0, s0
	v_lshl_add_u32 v236, s42, 13, v221
	s_waitcnt vmcnt(6) lgkmcnt(0)
	s_barrier
	ds_read_b128 v[4:7], v236
	s_lshl_b32 s2, s40, 12
	v_add_u32_e32 v233, s2, v222
	s_lshl_b32 s1, s1, 2
	s_add_i32 s50, s1, 0
	s_add_i32 s50, s50, 0x18000
	s_add_u32 s2, s20, 0x60000
	s_addc_u32 s3, s21, 0
	v_mov_b32_e32 v3, v2
	v_mov_b32_e32 v12, v2
	v_mov_b32_e32 v13, v2
	s_movk_i32 s57, 0x4000
	s_mov_b32 s0, 0
	s_mov_b32 s55, 0x8000
	v_lshl_add_u32 v232, v217, 2, s50
	v_mov_b32_e32 v238, 0
	s_mov_b32 s56, -1
	s_waitcnt vmcnt(3) lgkmcnt(0)
	v_mfma_f32_32x32x16_bf16 v[50:65], v[4:7], v[66:69], v[34:49]
	ds_read_b128 v[4:7], v236 offset:512
	s_waitcnt lgkmcnt(0)
	v_mfma_f32_32x32x16_bf16 v[34:49], v[4:7], v[66:69], v[34:49]
	ds_read_b128 v[4:7], v236 offset:2048
	s_waitcnt vmcnt(2) lgkmcnt(0)
	v_mfma_f32_32x32x16_bf16 v[50:65], v[4:7], v[70:73], v[50:65]
	ds_read_b128 v[4:7], v236 offset:2560
	s_waitcnt lgkmcnt(0)
	v_mfma_f32_32x32x16_bf16 v[34:49], v[4:7], v[70:73], v[34:49]
	ds_read_b128 v[4:7], v236 offset:4096
	ds_read_b128 v[8:11], v236 offset:4608
	ds_read_b128 v[82:85], v236 offset:6656
	ds_read_b128 v[14:17], v236 offset:6144
	s_waitcnt vmcnt(1) lgkmcnt(3)
	v_mfma_f32_32x32x16_bf16 v[50:65], v[4:7], v[74:77], v[50:65]
	v_mov_b32_e32 v4, v2
	v_mov_b32_e32 v5, v2
	v_mov_b32_e32 v6, v2
	v_mov_b32_e32 v7, v2
	s_waitcnt lgkmcnt(2)
	v_mfma_f32_32x32x16_bf16 v[34:49], v[8:11], v[74:77], v[34:49]
	v_mov_b32_e32 v8, v2
	v_mov_b32_e32 v9, v2
	v_mov_b32_e32 v10, v2
	v_mov_b32_e32 v11, v2
	s_waitcnt vmcnt(0) lgkmcnt(0)
	v_mfma_f32_32x32x16_bf16 v[50:65], v[14:17], v[78:81], v[50:65]
	v_mov_b32_e32 v16, v2
	v_mov_b32_e32 v17, v2
	v_mov_b32_e32 v14, v2
	v_mov_b32_e32 v15, v2
	v_mfma_f32_32x32x16_bf16 v[34:49], v[82:85], v[78:81], v[34:49]
	s_nop 15
	s_nop 7
	ds_write_b128 v233, v[66:69]
	ds_write_b128 v233, v[70:73] offset:1024
	ds_write_b128 v233, v[74:77] offset:2048
	ds_write_b128 v233, v[78:81] offset:3072
	v_max3_f32 v66, v50, v51, v34
	v_max3_f32 v67, v52, v53, v35
	v_mov_b64_e32 v[96:97], v[16:17]
	v_max3_f32 v66, v66, v36, v37
	v_max3_f32 v67, v67, v56, v57
	v_mov_b64_e32 v[94:95], v[14:15]
	v_max3_f32 v66, v66, v54, v55
	v_max3_f32 v67, v67, v40, v41
	v_mov_b64_e32 v[92:93], v[12:13]
	v_max3_f32 v66, v66, v38, v39
	v_max3_f32 v67, v67, v60, v61
	v_mov_b64_e32 v[90:91], v[10:11]
	v_max3_f32 v66, v66, v58, v59
	v_max3_f32 v67, v67, v44, v45
	v_mov_b64_e32 v[88:89], v[8:9]
	v_max3_f32 v66, v66, v42, v43
	v_max3_f32 v67, v67, v64, v65
	v_mov_b64_e32 v[86:87], v[6:7]
	v_max3_f32 v66, v66, v62, v63
	v_max3_f32 v67, v67, v48, v49
	v_mov_b64_e32 v[84:85], v[4:5]
	v_max3_f32 v66, v66, v46, v47
	v_mov_b64_e32 v[82:83], v[2:3]
	v_max_f32_e32 v66, v66, v67
	s_nop 0
	v_mov_b32_e32 v67, v66
	s_nop 1
	v_permlane32_swap_b32_e32 v66, v67
	v_max_f32_e32 v66, v66, v67
	s_nop 0
	v_add_f32_e32 v234, v2, v66
	v_sub_f32_e32 v50, v50, v66
	v_sub_f32_e32 v34, v34, v66
	v_sub_f32_e32 v51, v51, v66
	v_sub_f32_e32 v35, v35, v66
	v_sub_f32_e32 v52, v52, v66
	s_nop 0
	v_xor_b32_e32 v98, 0x80000000, v234
	v_mov_b32_e32 v99, v98
	v_mov_b32_e32 v100, v98
	v_mov_b32_e32 v101, v98
	v_mov_b32_e32 v102, v98
	v_mov_b32_e32 v103, v98
	v_mov_b32_e32 v104, v98
	v_mov_b32_e32 v105, v98
	v_mov_b32_e32 v106, v98
	v_mov_b32_e32 v107, v98
	v_mov_b32_e32 v108, v98
	v_mov_b32_e32 v109, v98
	v_mov_b32_e32 v110, v98
	v_mov_b32_e32 v111, v98
	v_mov_b32_e32 v112, v98
	v_mov_b32_e32 v113, v98
	s_waitcnt vmcnt(0) lgkmcnt(0)
	s_barrier
; #define WAIT_BAR(N) asm volatile("s_waitcnt vmcnt(" #N ") lgkmcnt(0)\n\ts_barrier" ::: "memory")
; #define DMA_K(t, slot) do { const bf16_t* sb_ = Kh + (long)(t) * KVBLK * DMK; glds16<0>(sb_, kvoff, (unsigned)__builtin_amdgcn_readfirstlane(kdst + (slot))); glds16<0>(sb_ + 64, kvoff, (unsigned)__builtin_amdgcn_readfirstlane(kdst + 8192 + (slot))); } while (0)
; #define DMA_V(t, slot) do { const bf16_t* sb_ = Vh + (long)(t) * KVBLK * DMK; glds16<0>(sb_, vvoff, (unsigned)__builtin_amdgcn_readfirstlane(vdst + (slot))); glds16<0>(sb_ + 64, vvoff, (unsigned)__builtin_amdgcn_readfirstlane(vdst + 8192 + (slot))); } while (0)
; #define ROT() do { sl_prev = sl_cur; sl_cur = sl_next; sl_next = (sl_next == (NSLOT - 1) * SLOTB) ? 0 : sl_next + SLOTB; } while (0)
; template <int THRL> ...
;     ...
;   START(pA0, pA1);
; #pragma unroll
;   for (int r = 0; r < 16; ++r) pA1[r] = __builtin_amdgcn_exp2f(pA1[r]);
;   WAIT_BAR(0);
;   DMA_K(3, 0); DMA_V(1, SLOTB);
;   ROT();
;   kload8(kf, kp0 + sl_cur);
;   WAIT_BAR(4);
;   s16x4 vlo[4], vhi[4]; u32x4 pw0, pw1, pw2, pw3;
	s_mov_b32 s1, m0
	s_mov_b32 m0, s49
	s_nop 0
	global_load_lds_dwordx4 v237, s[2:3] offset:0
	s_mov_b32 m0, s1
	s_add_u32 s2, s20, 0x60080
	s_addc_u32 s3, s21, 0
	s_mov_b32 s1, m0
	s_mov_b32 m0, s54
	s_nop 0
	global_load_lds_dwordx4 v237, s[2:3] offset:0
	s_mov_b32 m0, s1
	s_add_u32 s2, s8, 0x20000
	s_addc_u32 s3, s9, 0
	s_add_i32 s44, s49, 0x10000
	s_mov_b32 s1, m0
	s_mov_b32 m0, s44
	s_nop 0
	global_load_lds_dwordx4 v235, s[2:3] offset:0
	s_mov_b32 m0, s1
	s_add_u32 s2, s8, 0x20080
	s_addc_u32 s3, s9, 0
	s_add_i32 s43, s49, 0x12000
	s_mov_b32 s1, m0
	s_mov_b32 m0, s43
	s_nop 0
	global_load_lds_dwordx4 v235, s[2:3] offset:0
	s_mov_b32 m0, s1
	ds_read_b128 v[146:149], v236 offset:16384
	ds_read_b128 v[202:205], v236 offset:16896
	ds_read_b128 v[206:209], v236 offset:18432
	ds_read_b128 v[190:193], v236 offset:18944
	ds_read_b128 v[198:201], v236 offset:20480
	ds_read_b128 v[186:189], v236 offset:20992
	ds_read_b128 v[182:185], v236 offset:22528
	ds_read_b128 v[178:181], v236 offset:23040
	v_sub_f32_e32 v36, v36, v66
	v_sub_f32_e32 v53, v53, v66
	v_sub_f32_e32 v37, v37, v66
	v_sub_f32_e32 v54, v54, v66
	v_sub_f32_e32 v38, v38, v66
	v_sub_f32_e32 v55, v55, v66
	v_sub_f32_e32 v39, v39, v66
	v_sub_f32_e32 v56, v56, v66
	v_sub_f32_e32 v40, v40, v66
	v_sub_f32_e32 v57, v57, v66
	v_sub_f32_e32 v41, v41, v66
	v_sub_f32_e32 v58, v58, v66
	v_sub_f32_e32 v42, v42, v66
	v_sub_f32_e32 v59, v59, v66
	v_sub_f32_e32 v43, v43, v66
	v_sub_f32_e32 v60, v60, v66
	v_sub_f32_e32 v44, v44, v66
	v_sub_f32_e32 v61, v61, v66
	v_sub_f32_e32 v45, v45, v66
	v_sub_f32_e32 v62, v62, v66
	v_sub_f32_e32 v46, v46, v66
	v_sub_f32_e32 v63, v63, v66
	v_sub_f32_e32 v47, v47, v66
	v_sub_f32_e32 v64, v64, v66
	v_sub_f32_e32 v48, v48, v66
	v_sub_f32_e32 v65, v65, v66
	v_sub_f32_e32 v49, v49, v66
	v_exp_f32_e32 v130, v50
	v_exp_f32_e32 v131, v51
	v_exp_f32_e32 v132, v52
	v_exp_f32_e32 v133, v53
	v_exp_f32_e32 v134, v54
	v_exp_f32_e32 v135, v55
	v_exp_f32_e32 v136, v56
	v_exp_f32_e32 v137, v57
	v_exp_f32_e32 v138, v58
	v_exp_f32_e32 v139, v59
	v_exp_f32_e32 v140, v60
	v_exp_f32_e32 v141, v61
	v_exp_f32_e32 v142, v62
	v_exp_f32_e32 v143, v63
	v_exp_f32_e32 v144, v64
	v_exp_f32_e32 v145, v65
	v_exp_f32_e32 v114, v34
	v_exp_f32_e32 v115, v35
	v_exp_f32_e32 v116, v36
	v_exp_f32_e32 v117, v37
	v_exp_f32_e32 v118, v38
	v_exp_f32_e32 v119, v39
	v_exp_f32_e32 v120, v40
	v_exp_f32_e32 v121, v41
	v_exp_f32_e32 v122, v42
	v_exp_f32_e32 v123, v43
	v_exp_f32_e32 v124, v44
	v_exp_f32_e32 v125, v45
	v_exp_f32_e32 v126, v46
	v_exp_f32_e32 v127, v47
	v_exp_f32_e32 v128, v48
	v_exp_f32_e32 v129, v49
	s_waitcnt vmcnt(4) lgkmcnt(0)
	s_barrier
	v_mov_b64_e32 v[80:81], v[16:17]
	v_mov_b64_e32 v[48:49], v[16:17]
	v_mov_b64_e32 v[64:65], v[16:17]
	v_mov_b64_e32 v[78:79], v[14:15]
	v_mov_b64_e32 v[76:77], v[12:13]
	v_mov_b64_e32 v[74:75], v[10:11]
	v_mov_b64_e32 v[72:73], v[8:9]
	v_mov_b64_e32 v[70:71], v[6:7]
	v_mov_b64_e32 v[68:69], v[4:5]
	v_mov_b64_e32 v[66:67], v[2:3]
	v_mov_b64_e32 v[46:47], v[14:15]
	v_mov_b64_e32 v[44:45], v[12:13]
	v_mov_b64_e32 v[42:43], v[10:11]
	v_mov_b64_e32 v[40:41], v[8:9]
	v_mov_b64_e32 v[38:39], v[6:7]
	v_mov_b64_e32 v[36:37], v[4:5]
	v_mov_b64_e32 v[34:35], v[2:3]
	v_mov_b64_e32 v[62:63], v[14:15]
	v_mov_b64_e32 v[60:61], v[12:13]
	v_mov_b64_e32 v[58:59], v[10:11]
	v_mov_b64_e32 v[56:57], v[8:9]
	v_mov_b64_e32 v[54:55], v[6:7]
	v_mov_b64_e32 v[52:53], v[4:5]
	v_mov_b64_e32 v[50:51], v[2:3]
	v_mov_b32_e32 v244, 0x23ee8
	ds_read2_b64 v[250:253], v244 offset1:1
	ds_read_b64 v[254:255], v244 offset:16
	s_waitcnt lgkmcnt(0)
	v_readfirstlane_b32 s68, v250
	v_readfirstlane_b32 s69, v251
	v_readfirstlane_b32 s70, v252
	v_readfirstlane_b32 s71, v253
	v_readfirstlane_b32 s72, v254
	v_readfirstlane_b32 s73, v255
	ds_read_b64 v[250:251], v244 offset:40
	s_waitcnt lgkmcnt(0)
	v_readfirstlane_b32 s74, v250
	v_readfirstlane_b32 s75, v251
	s_add_u32 s76, s74, 0x16530000
	s_addc_u32 s77, s75, 0
	s_add_u32 s74, s74, 0xa530000
	s_addc_u32 s75, s75, 0
	v_lshrrev_b32_e32 v25, 3, v214
	v_and_b32_e32 v28, 7, v214
	v_lshlrev_b32_e32 v33, 4, v28
	v_lshl_add_u32 v24, v25, 12, v33
	v_lshl_add_u32 v246, v25, 13, v33
	v_lshlrev_b32_e32 v29, 8, v28
	v_lshl_add_u32 v29, v25, 1, v29
	s_lshl_b32 s2, s40, 11
	s_cmp_lt_u32 s40, 6
	s_mov_b32 s3, 0x21000
	s_cselect_b32 s3, 0x20800, s3
	s_add_i32 s2, s2, s3
	v_add_u32_e32 v29, s2, v29
	v_add_u32_e32 v29, 32, v29
	v_lshl_add_u32 v32, v214, 3, s2
	s_mul_i32 s66, s96, 8
	s_add_i32 s66, s66, s40
	s_cmpk_lt_u32 s36, 0x100
	s_movk_i32 s67, 104
	s_cselect_b32 s67, 104, s67
	s_cselect_b32 s2, 0, 0x6800
	s_add_i32 s66, s66, s2
	s_add_i32 s90, s67, 6
	s_cmp_eq_u32 s67, 0
	s_cselect_b32 s90, -1, s90
	global_load_dword v249, v24, s[68:69]
	global_load_dword v249, v24, s[68:69]

; __device__ __forceinline__ void convert_moe_items(const Ctx& a, int layer, LAS unsigned char* lds, int it0, int it1, int widx, int nw, int wave, int lane) {
;     ...
;     auto decode = [&](int it) { CvtItem d; const int e = it / PER_E; int r = it % PER_E; const size_t eo = ((size_t)layer * NE + e) * (size_t)DM * FE;
;         if (r < I_G)          { d.src = wg + eo; d.dst = WGU; d.N = FE; d.K = DM; d.row_off = e * 2048; d.ilv = 1; }
;         else if (r < 2 * I_G) { r -= I_G; d.src = wu + eo; d.dst = WGU; d.N = FE; d.K = DM; d.row_off = e * 2048 + 128; d.ilv = 1; }
;         else                  { r -= 2 * I_G; d.src = wd + eo; d.dst = WD; d.N = DM; d.K = FE; d.row_off = e * 2048; d.ilv = 0; }
;         const int nblk = d.N / 32; d.k0 = 64 * (r / nblk); d.n0 = 32 * (r % nblk); return d; };
.Lcs_dec_h0:
	s_cmp_lt_u32 s66, 0xa800
	s_cbranch_scc1 .Lcs_id_h0
	s_bitcmp1_b32 s66, 16
	s_cbranch_scc1 .Lcs_id_h0
	s_add_i32 s66, s66, 0xf000
.Lcs_id_h0:
	s_and_b32 s3, s66, 0xffff
	s_lshr_b32 s91, s66, 16
	s_mul_i32 s78, s3, 0xaaab
	s_lshr_b32 s78, s78, 27
	s_mul_i32 s79, s78, 0xc00
	s_sub_i32 s79, s3, s79
	s_addk_i32 s66, 0x800
	s_xor_b32 s80, s91, 1
	s_lshl_b32 s80, s80, 4
	s_add_i32 s80, s80, s78
	s_lshl_b32 s80, s80, 23
	s_lshl_b32 s91, s91, 27
	s_lshl_b32 s81, s78, 11
	s_cmpk_gt_u32 s79, 0x7ff
	s_cbranch_scc1 .Lcs_down_h0
	s_mov_b64 s[98:99], s[68:69]
	s_cmpk_gt_u32 s79, 0x3ff
	s_cbranch_scc0 .Lcs_gate_h0
	s_mov_b64 s[98:99], s[70:71]
	s_addk_i32 s81, 0x80
	s_addk_i32 s79, 0xfc00
.Lcs_gate_h0:
	s_add_u32 s98, s98, s80
	s_addc_u32 s99, s99, 0
	s_lshr_b32 s82, s79, 5
	s_lshl_b32 s82, s82, 6
	s_and_b32 s83, s79, 31
	s_lshl_b32 s83, s83, 5
	s_lshl_b32 s84, s82, 12
	s_lshl_b32 s85, s83, 2
	s_add_i32 s84, s84, s85
	s_add_u32 s98, s98, s84
	s_addc_u32 s99, s99, 0
	s_mov_b32 s62, 0x8000
	s_mov_b32 s88, 0x8000
	s_mov_b32 s89, 0x17fc0
	s_lshr_b32 s84, s83, 7
	s_lshl_b32 s84, s84, 8
	s_and_b32 s85, s83, 0x7f
	s_add_i32 s84, s84, s85
	s_add_i32 s84, s84, s81
	s_lshl_b32 s84, s84, 12
	s_lshl_b32 s85, s82, 1
	s_add_i32 s84, s84, s85
	s_add_u32 s64, s74, s84
	s_addc_u32 s65, s75, 0
	s_sub_u32 s64, s64, s91
	s_subb_u32 s65, s65, 0
	v_mov_b32_e32 v25, v24
	v_lshrrev_b32_e32 v33, 1, v246
	s_branch .Lcs_Lgo_h0
.Lcs_down_h0:
	s_addk_i32 s79, 0xf800
	s_add_u32 s98, s72, s80
	s_addc_u32 s99, s73, 0
	s_lshr_b32 s82, s79, 6
	s_lshl_b32 s82, s82, 6
	s_and_b32 s83, s79, 63
	s_lshl_b32 s83, s83, 5
	s_lshl_b32 s84, s82, 13
	s_lshl_b32 s85, s83, 2
	s_add_i32 s84, s84, s85
	s_add_u32 s98, s98, s84
	s_addc_u32 s99, s99, 0
	s_mov_b32 s62, 0x10000
	s_mov_b32 s88, 0x4000
	s_mov_b32 s89, 0xbfc0
	s_add_i32 s84, s81, s83
	s_lshl_b32 s84, s84, 11
	s_lshl_b32 s85, s82, 1
	s_add_i32 s84, s84, s85
	s_add_u32 s64, s76, s84
	s_addc_u32 s65, s77, 0
	s_lshr_b32 s91, s91, 1
	s_sub_u32 s64, s64, s91
	s_subb_u32 s65, s65, 0
	v_mov_b32_e32 v25, v246
	v_lshrrev_b32_e32 v33, 1, v24
	s_branch .Lcs_Lgo_h0

; #define LAS __attribute__((address_space(3)))
;     __device__ __forceinline__ const float* x() const { return (const float*)ld(0); }
; __global__ void __launch_bounds__(NTHR, 2) fwd(Args ka) {
;     extern __shared__ __attribute__((aligned(16))) unsigned char lds_raw[];
;     LAS unsigned char* lds = (LAS unsigned char*)lds_raw;
;     const int tid = threadIdx.x;
	.amdhsa_kernel _Z3fwd4Args
		.amdhsa_group_segment_fixed_size 4096
		.amdhsa_private_segment_fixed_size 0
		.amdhsa_kernarg_size 480
		.amdhsa_user_sgpr_count 2
		.amdhsa_user_sgpr_dispatch_ptr 0
		.amdhsa_user_sgpr_queue_ptr 0
		.amdhsa_user_sgpr_kernarg_segment_ptr 1
		.amdhsa_user_sgpr_dispatch_id 0
		.amdhsa_user_sgpr_kernarg_preload_length 0
		.amdhsa_user_sgpr_kernarg_preload_offset 0
		.amdhsa_user_sgpr_private_segment_size 0
		.amdhsa_uses_dynamic_stack 0
		.amdhsa_enable_private_segment 0
		.amdhsa_system_sgpr_workgroup_id_x 1
		.amdhsa_system_sgpr_workgroup_id_y 0
		.amdhsa_system_sgpr_workgroup_id_z 0
		.amdhsa_system_sgpr_workgroup_info 0
		.amdhsa_system_vgpr_workitem_id 0
		.amdhsa_next_free_vgpr 256
		.amdhsa_next_free_sgpr 102
		.amdhsa_accum_offset 256
		.amdhsa_reserve_vcc 1
		.amdhsa_float_round_mode_32 0
		.amdhsa_float_round_mode_16_64 0
		.amdhsa_float_denorm_mode_32 3
		.amdhsa_float_denorm_mode_16_64 3
		.amdhsa_dx10_clamp 1
		.amdhsa_ieee_mode 1
		.amdhsa_fp16_overflow 0
		.amdhsa_tg_split 0
		.amdhsa_exception_fp_ieee_invalid_op 0
		.amdhsa_exception_fp_denorm_src 0
		.amdhsa_exception_fp_ieee_div_zero 0
		.amdhsa_exception_fp_ieee_overflow 0
		.amdhsa_exception_fp_ieee_underflow 0
		.amdhsa_exception_fp_ieee_inexact 0
		.amdhsa_exception_int_div_zero 0
	.end_amdhsa_kernel

; #define LAS __attribute__((address_space(3)))
;     __device__ __forceinline__ const float* x() const { return (const float*)ld(0); }
; __global__ void __launch_bounds__(NTHR, 2) fwd(Args ka) {
;     extern __shared__ __attribute__((aligned(16))) unsigned char lds_raw[];
;     LAS unsigned char* lds = (LAS unsigned char*)lds_raw;
;     const int tid = threadIdx.x;
amdhsa.kernels:
  - .agpr_count:     0
    .args:
      - .offset:         0
        .size:           224
        .value_kind:     by_value
      - .offset:         224
        .size:           4
        .value_kind:     hidden_block_count_x
      - .offset:         228
        .size:           4
        .value_kind:     hidden_block_count_y
      - .offset:         232
        .size:           4
        .value_kind:     hidden_block_count_z
      - .offset:         236
        .size:           2
        .value_kind:     hidden_group_size_x
      - .offset:         238
        .size:           2
        .value_kind:     hidden_group_size_y
      - .offset:         240
        .size:           2
        .value_kind:     hidden_group_size_z
      - .offset:         242
        .size:           2
        .value_kind:     hidden_remainder_x
      - .offset:         244
        .size:           2
        .value_kind:     hidden_remainder_y
      - .offset:         246
        .size:           2
        .value_kind:     hidden_remainder_z
      - .offset:         264
        .size:           8
        .value_kind:     hidden_global_offset_x
      - .offset:         272
        .size:           8
        .value_kind:     hidden_global_offset_y
      - .offset:         280
        .size:           8
        .value_kind:     hidden_global_offset_z
      - .offset:         288
        .size:           2
        .value_kind:     hidden_grid_dims
      - .offset:         344
        .size:           4
        .value_kind:     hidden_dynamic_lds_size
    .group_segment_fixed_size: 4096
    .kernarg_segment_align: 8
    .kernarg_segment_size: 480
    .language:       OpenCL C
    .language_version:
      - 2
      - 0
    .max_flat_workgroup_size: 512
    .name:           _Z3fwd4Args
    .private_segment_fixed_size: 0
    .sgpr_count:     108
    .sgpr_spill_count: 25
    .symbol:         _Z3fwd4Args.kd
    .uniform_work_group_size: 1
    .uses_dynamic_stack: false
    .vgpr_count:     256
    .vgpr_spill_count: 0
    .wavefront_size: 64
